# speedup vs baseline: 1.0087x; 1.0015x over previous
.Lmk_start:
	s_mov_b32 s28, s8
	s_mov_b64 s[30:31], s[4:5]
	s_mov_b64 s[32:33], s[6:7]
	s_mov_b64 s[6:7], s[2:3]
	s_mov_b32 s2, s28
	s_and_b32 s3, s2, 7
	s_lshr_b32 s4, s2, 3
	s_and_b32 s5, s4, 3
	s_lshl_b32 s3, s3, 2
	s_or_b32 s8, s3, s5
	s_lshr_b32 s9, s4, 2
	v_lshrrev_b32_e32 v127, 6, v0
	v_and_b32_e32 v124, 63, v0
	v_lshlrev_b32_e32 v125, 3, v124
	v_lshlrev_b32_e32 v124, 4, v124
	v_readfirstlane_b32 s12, v127
	v_mov_b32_e32 v120, 0
	v_mov_b32_e32 v121, 0
	v_mov_b32_e32 v122, 0
	v_mov_b32_e32 v123, 0
	s_lshl_b32 s13, s12, 10
	s_lshl_b32 s14, s9, 3
	s_add_u32 s14, s14, s12
	s_mul_i32 s15, s14, 0x1800
	s_mul_i32 s16, s8, 0x12000
	s_add_u32 s16, s16, 0xc0000
	s_add_u32 s16, s16, s13
	s_add_u32 s20, s13, 0x2000
	s_add_u32 s10, s6, s16
	s_addc_u32 s11, s7, 0
	s_add_u32 s18, s6, s15
	s_addc_u32 s19, s7, 0
	s_add_u32 s22, s18, 0x1000
	s_addc_u32 s23, s19, 0
	s_cmp_lt_u32 s12, 4
	s_cbranch_scc0 .Lmk_vb
	s_mov_b32 m0, s13
	s_nop 0
	global_load_lds_dwordx4 v124, s[10:11]
	s_add_u32 s26, s10, 0x2000
	s_addc_u32 s27, s11, 0
	s_mov_b32 m0, s20
	s_nop 0
	global_load_lds_dwordx4 v124, s[26:27]
	global_load_dwordx4 v[96:99], v124, s[18:19]
	global_load_dwordx2 v[100:101], v125, s[22:23]
	global_load_dwordx4 v[102:105], v124, s[18:19] offset:1024
	global_load_dwordx2 v[106:107], v125, s[22:23] offset:512
	global_load_dwordx4 v[108:111], v124, s[18:19] offset:2048
	global_load_dwordx2 v[112:113], v125, s[22:23] offset:1024
	global_load_dwordx4 v[114:117], v124, s[18:19] offset:3072
	global_load_dwordx2 v[118:119], v125, s[22:23] offset:1536
	s_add_u32 s24, s10, 0x3000
	s_addc_u32 s25, s11, 0
	s_add_u32 s26, s13, 0x3000
	s_mov_b32 m0, s26
	s_nop 0
	global_load_lds_dwordx4 v124, s[24:25]
	s_add_u32 s26, s24, 0x2000
	s_addc_u32 s27, s25, 0
	s_add_u32 s29, s20, 0x3000
	s_mov_b32 m0, s29
	s_nop 0
	global_load_lds_dwordx4 v124, s[26:27]
	s_add_u32 s24, s10, 0x6000
	s_addc_u32 s25, s11, 0
	s_add_u32 s26, s13, 0x6000
	s_mov_b32 m0, s26
	s_nop 0
	global_load_lds_dwordx4 v124, s[24:25]
	s_add_u32 s26, s24, 0x2000
	s_addc_u32 s27, s25, 0
	s_add_u32 s29, s20, 0x6000
	s_mov_b32 m0, s29
	s_nop 0
	global_load_lds_dwordx4 v124, s[26:27]
	s_add_u32 s24, s10, 0x9000
	s_addc_u32 s25, s11, 0
	s_add_u32 s26, s13, 0x9000
	s_mov_b32 m0, s26
	s_nop 0
	global_load_lds_dwordx4 v124, s[24:25]
	s_add_u32 s26, s24, 0x2000
	s_addc_u32 s27, s25, 0
	s_add_u32 s29, s20, 0x9000
	s_mov_b32 m0, s29
	s_nop 0
	global_load_lds_dwordx4 v124, s[26:27]
	s_add_u32 s24, s10, 0xc000
	s_addc_u32 s25, s11, 0
	s_add_u32 s26, s13, 0xc000
	s_mov_b32 m0, s26
	s_nop 0
	global_load_lds_dwordx4 v124, s[24:25]
	s_add_u32 s26, s24, 0x2000
	s_addc_u32 s27, s25, 0
	s_add_u32 s29, s20, 0xc000
	s_mov_b32 m0, s29
	s_nop 0
	global_load_lds_dwordx4 v124, s[26:27]
	s_waitcnt vmcnt(8)
	s_barrier
	ds_read_b128 v[0:3], v124
	ds_read_b64 v[4:5], v125 offset:4096
	ds_read_b128 v[6:9], v124 offset:1024
	ds_read_b64 v[10:11], v125 offset:4608
	ds_read_b128 v[12:15], v124 offset:2048
	ds_read_b64 v[16:17], v125 offset:5120
	ds_read_b128 v[18:21], v124 offset:3072
	ds_read_b64 v[22:23], v125 offset:5632
	s_waitcnt lgkmcnt(0)
	s_setprio 3
	v_mfma_f32_32x32x64_f8f6f4 v[48:63], v[0:5], v[96:101], 0 cbsz:2 blgp:2
	ds_read_b128 v[24:27], v124 offset:6144
	ds_read_b64 v[28:29], v125 offset:10240
	v_mfma_f32_32x32x64_f8f6f4 v[48:63], v[6:11], v[102:107], v[48:63] cbsz:2 blgp:2
	ds_read_b128 v[30:33], v124 offset:7168
	ds_read_b64 v[34:35], v125 offset:10752
	v_mfma_f32_32x32x64_f8f6f4 v[48:63], v[12:17], v[108:113], v[48:63] cbsz:2 blgp:2
	ds_read_b128 v[36:39], v124 offset:8192
	ds_read_b64 v[40:41], v125 offset:11264
	v_mfma_f32_32x32x64_f8f6f4 v[48:63], v[18:23], v[114:119], v[48:63] cbsz:2 blgp:2
	ds_read_b128 v[42:45], v124 offset:9216
	ds_read_b64 v[46:47], v125 offset:11776
	s_waitcnt vmcnt(6) lgkmcnt(0)
	s_barrier
	s_add_u32 s24, s10, 0xf000
	s_addc_u32 s25, s11, 0
	s_mov_b32 m0, s13
	s_nop 0
	global_load_lds_dwordx4 v124, s[24:25]
	s_add_u32 s26, s24, 0x2000
	s_addc_u32 s27, s25, 0
	s_mov_b32 m0, s20
	s_nop 0
	global_load_lds_dwordx4 v124, s[26:27]
	v_mfma_f32_32x32x64_f8f6f4 v[64:79], v[24:29], v[96:101], 0 cbsz:2 blgp:2
	ds_read_b128 v[0:3], v124 offset:12288
	ds_read_b64 v[4:5], v125 offset:16384
	ds_read_b128 v[6:9], v124 offset:13312
	ds_read_b64 v[10:11], v125 offset:16896
	ds_read_b128 v[24:27], v124 offset:18432
	ds_read_b64 v[28:29], v125 offset:22528
	v_mfma_f32_32x32x64_f8f6f4 v[64:79], v[30:35], v[102:107], v[64:79] cbsz:2 blgp:2
	ds_read_b128 v[12:15], v124 offset:14336
	ds_read_b64 v[16:17], v125 offset:17408
	ds_read_b128 v[18:21], v124 offset:15360
	ds_read_b64 v[22:23], v125 offset:17920
	ds_read_b128 v[30:33], v124 offset:19456
	ds_read_b64 v[34:35], v125 offset:23040
	v_exp_f32_e32 v48, v48
	v_exp_f32_e32 v49, v49
	v_exp_f32_e32 v50, v50
	v_exp_f32_e32 v51, v51
	v_mfma_f32_32x32x64_f8f6f4 v[64:79], v[36:41], v[108:113], v[64:79] cbsz:2 blgp:2
	ds_read_b128 v[36:39], v124 offset:20480
	ds_read_b64 v[40:41], v125 offset:23552
	v_exp_f32_e32 v52, v52
	v_exp_f32_e32 v53, v53
	v_exp_f32_e32 v54, v54
	v_exp_f32_e32 v55, v55
	v_pk_add_f32 v[120:121], v[120:121], v[48:49]
	v_pk_add_f32 v[122:123], v[122:123], v[50:51]
	v_mfma_f32_32x32x64_f8f6f4 v[64:79], v[42:47], v[114:119], v[64:79] cbsz:2 blgp:2
	ds_read_b128 v[42:45], v124 offset:21504
	ds_read_b64 v[46:47], v125 offset:24064
	v_exp_f32_e32 v56, v56
	v_exp_f32_e32 v57, v57
	v_exp_f32_e32 v58, v58
	v_exp_f32_e32 v59, v59
	v_pk_add_f32 v[120:121], v[120:121], v[52:53]
	v_pk_add_f32 v[122:123], v[122:123], v[54:55]
	s_waitcnt vmcnt(6) lgkmcnt(6)
	s_barrier
	v_mfma_f32_32x32x64_f8f6f4 v[80:95], v[0:5], v[96:101], 0 cbsz:2 blgp:2
	ds_read_b128 v[0:3], v124 offset:24576
	ds_read_b64 v[4:5], v125 offset:28672
	v_exp_f32_e32 v60, v60
	v_exp_f32_e32 v61, v61
	v_exp_f32_e32 v62, v62
	v_exp_f32_e32 v63, v63
	v_pk_add_f32 v[120:121], v[120:121], v[56:57]
	v_pk_add_f32 v[122:123], v[122:123], v[58:59]
	v_mfma_f32_32x32x64_f8f6f4 v[80:95], v[6:11], v[102:107], v[80:95] cbsz:2 blgp:2
	ds_read_b128 v[6:9], v124 offset:25600
	ds_read_b64 v[10:11], v125 offset:29184
	v_exp_f32_e32 v64, v64
	v_exp_f32_e32 v65, v65
	v_exp_f32_e32 v66, v66
	v_exp_f32_e32 v67, v67
	v_pk_add_f32 v[120:121], v[120:121], v[60:61]
	v_pk_add_f32 v[122:123], v[122:123], v[62:63]
	v_mfma_f32_32x32x64_f8f6f4 v[80:95], v[12:17], v[108:113], v[80:95] cbsz:2 blgp:2
	ds_read_b128 v[12:15], v124 offset:26624
	ds_read_b64 v[16:17], v125 offset:29696
	v_exp_f32_e32 v68, v68
	v_exp_f32_e32 v69, v69
	v_exp_f32_e32 v70, v70
	v_exp_f32_e32 v71, v71
	v_pk_add_f32 v[120:121], v[120:121], v[64:65]
	v_pk_add_f32 v[122:123], v[122:123], v[66:67]
	v_mfma_f32_32x32x64_f8f6f4 v[80:95], v[18:23], v[114:119], v[80:95] cbsz:2 blgp:2
	ds_read_b128 v[18:21], v124 offset:27648
	ds_read_b64 v[22:23], v125 offset:30208
	v_exp_f32_e32 v72, v72
	v_exp_f32_e32 v73, v73
	v_exp_f32_e32 v74, v74
	v_exp_f32_e32 v75, v75
	v_pk_add_f32 v[120:121], v[120:121], v[68:69]
	v_pk_add_f32 v[122:123], v[122:123], v[70:71]
	s_waitcnt lgkmcnt(8)
	s_nop 0
	v_mfma_f32_32x32x64_f8f6f4 v[48:63], v[24:29], v[96:101], 0 cbsz:2 blgp:2
	ds_read_b128 v[24:27], v124 offset:30720
	ds_read_b64 v[28:29], v125 offset:34816
	v_exp_f32_e32 v76, v76
	v_exp_f32_e32 v77, v77
	v_exp_f32_e32 v78, v78
	v_exp_f32_e32 v79, v79
	v_pk_add_f32 v[120:121], v[120:121], v[72:73]
	v_pk_add_f32 v[122:123], v[122:123], v[74:75]
	v_mfma_f32_32x32x64_f8f6f4 v[48:63], v[30:35], v[102:107], v[48:63] cbsz:2 blgp:2
	ds_read_b128 v[30:33], v124 offset:31744
	ds_read_b64 v[34:35], v125 offset:35328
	v_exp_f32_e32 v80, v80
	v_exp_f32_e32 v81, v81
	v_exp_f32_e32 v82, v82
	v_exp_f32_e32 v83, v83
	v_pk_add_f32 v[120:121], v[120:121], v[76:77]
	v_pk_add_f32 v[122:123], v[122:123], v[78:79]
	v_mfma_f32_32x32x64_f8f6f4 v[48:63], v[36:41], v[108:113], v[48:63] cbsz:2 blgp:2
	ds_read_b128 v[36:39], v124 offset:32768
	ds_read_b64 v[40:41], v125 offset:35840
	v_exp_f32_e32 v84, v84
	v_exp_f32_e32 v85, v85
	v_exp_f32_e32 v86, v86
	v_exp_f32_e32 v87, v87
	v_pk_add_f32 v[120:121], v[120:121], v[80:81]
	v_pk_add_f32 v[122:123], v[122:123], v[82:83]
	v_mfma_f32_32x32x64_f8f6f4 v[48:63], v[42:47], v[114:119], v[48:63] cbsz:2 blgp:2
	ds_read_b128 v[42:45], v124 offset:33792
	ds_read_b64 v[46:47], v125 offset:36352
	v_exp_f32_e32 v88, v88
	v_exp_f32_e32 v89, v89
	v_exp_f32_e32 v90, v90
	v_exp_f32_e32 v91, v91
	v_pk_add_f32 v[120:121], v[120:121], v[84:85]
	v_pk_add_f32 v[122:123], v[122:123], v[86:87]
	s_setprio 2
	s_waitcnt vmcnt(4) lgkmcnt(8)
	s_barrier
	s_nop 0
	v_mfma_f32_32x32x64_f8f6f4 v[64:79], v[0:5], v[96:101], 0 cbsz:2 blgp:2
	ds_read_b128 v[0:3], v124 offset:36864
	ds_read_b64 v[4:5], v125 offset:40960
	v_exp_f32_e32 v92, v92
	v_exp_f32_e32 v93, v93
	v_exp_f32_e32 v94, v94
	v_exp_f32_e32 v95, v95
	v_pk_add_f32 v[120:121], v[120:121], v[88:89]
	v_pk_add_f32 v[122:123], v[122:123], v[90:91]
	v_mfma_f32_32x32x64_f8f6f4 v[64:79], v[6:11], v[102:107], v[64:79] cbsz:2 blgp:2
	ds_read_b128 v[6:9], v124 offset:37888
	ds_read_b64 v[10:11], v125 offset:41472
	v_exp_f32_e32 v48, v48
	v_exp_f32_e32 v49, v49
	v_exp_f32_e32 v50, v50
	v_exp_f32_e32 v51, v51
	v_pk_add_f32 v[120:121], v[120:121], v[92:93]
	v_pk_add_f32 v[122:123], v[122:123], v[94:95]
	v_mfma_f32_32x32x64_f8f6f4 v[64:79], v[12:17], v[108:113], v[64:79] cbsz:2 blgp:2
	ds_read_b128 v[12:15], v124 offset:38912
	ds_read_b64 v[16:17], v125 offset:41984
	v_exp_f32_e32 v52, v52
	v_exp_f32_e32 v53, v53
	v_exp_f32_e32 v54, v54
	v_exp_f32_e32 v55, v55
	v_pk_add_f32 v[120:121], v[120:121], v[48:49]
	v_pk_add_f32 v[122:123], v[122:123], v[50:51]
	v_mfma_f32_32x32x64_f8f6f4 v[64:79], v[18:23], v[114:119], v[64:79] cbsz:2 blgp:2
	ds_read_b128 v[18:21], v124 offset:39936
	ds_read_b64 v[22:23], v125 offset:42496
	v_exp_f32_e32 v56, v56
	v_exp_f32_e32 v57, v57
	v_exp_f32_e32 v58, v58
	v_exp_f32_e32 v59, v59
	v_pk_add_f32 v[120:121], v[120:121], v[52:53]
	v_pk_add_f32 v[122:123], v[122:123], v[54:55]
	s_waitcnt lgkmcnt(8)
	s_nop 0
	v_mfma_f32_32x32x64_f8f6f4 v[80:95], v[24:29], v[96:101], 0 cbsz:2 blgp:2
	ds_read_b128 v[24:27], v124 offset:43008
	ds_read_b64 v[28:29], v125 offset:47104
	v_exp_f32_e32 v60, v60
	v_exp_f32_e32 v61, v61
	v_exp_f32_e32 v62, v62
	v_exp_f32_e32 v63, v63
	v_pk_add_f32 v[120:121], v[120:121], v[56:57]
	v_pk_add_f32 v[122:123], v[122:123], v[58:59]
	v_mfma_f32_32x32x64_f8f6f4 v[80:95], v[30:35], v[102:107], v[80:95] cbsz:2 blgp:2
	ds_read_b128 v[30:33], v124 offset:44032
	ds_read_b64 v[34:35], v125 offset:47616
	v_exp_f32_e32 v64, v64
	v_exp_f32_e32 v65, v65
	v_exp_f32_e32 v66, v66
	v_exp_f32_e32 v67, v67
	v_pk_add_f32 v[120:121], v[120:121], v[60:61]
	v_pk_add_f32 v[122:123], v[122:123], v[62:63]
	v_mfma_f32_32x32x64_f8f6f4 v[80:95], v[36:41], v[108:113], v[80:95] cbsz:2 blgp:2
	ds_read_b128 v[36:39], v124 offset:45056
	ds_read_b64 v[40:41], v125 offset:48128
	v_exp_f32_e32 v68, v68
	v_exp_f32_e32 v69, v69
	v_exp_f32_e32 v70, v70
	v_exp_f32_e32 v71, v71
	v_pk_add_f32 v[120:121], v[120:121], v[64:65]
	v_pk_add_f32 v[122:123], v[122:123], v[66:67]
	v_mfma_f32_32x32x64_f8f6f4 v[80:95], v[42:47], v[114:119], v[80:95] cbsz:2 blgp:2
	ds_read_b128 v[42:45], v124 offset:46080
	ds_read_b64 v[46:47], v125 offset:48640
	v_exp_f32_e32 v72, v72
	v_exp_f32_e32 v73, v73
	v_exp_f32_e32 v74, v74
	v_exp_f32_e32 v75, v75
	v_pk_add_f32 v[120:121], v[120:121], v[68:69]
	v_pk_add_f32 v[122:123], v[122:123], v[70:71]
	s_waitcnt vmcnt(2) lgkmcnt(8)
	s_barrier
	v_mfma_f32_32x32x64_f8f6f4 v[48:63], v[0:5], v[96:101], 0 cbsz:2 blgp:2
	ds_read_b128 v[0:3], v124 offset:49152
	ds_read_b64 v[4:5], v125 offset:53248
	v_exp_f32_e32 v76, v76
	v_exp_f32_e32 v77, v77
	v_exp_f32_e32 v78, v78
	v_exp_f32_e32 v79, v79
	v_pk_add_f32 v[120:121], v[120:121], v[72:73]
	v_pk_add_f32 v[122:123], v[122:123], v[74:75]
	v_mfma_f32_32x32x64_f8f6f4 v[48:63], v[6:11], v[102:107], v[48:63] cbsz:2 blgp:2
	ds_read_b128 v[6:9], v124 offset:50176
	ds_read_b64 v[10:11], v125 offset:53760
	v_exp_f32_e32 v80, v80
	v_exp_f32_e32 v81, v81
	v_exp_f32_e32 v82, v82
	v_exp_f32_e32 v83, v83
	v_pk_add_f32 v[120:121], v[120:121], v[76:77]
	v_pk_add_f32 v[122:123], v[122:123], v[78:79]
	v_mfma_f32_32x32x64_f8f6f4 v[48:63], v[12:17], v[108:113], v[48:63] cbsz:2 blgp:2
	ds_read_b128 v[12:15], v124 offset:51200
	ds_read_b64 v[16:17], v125 offset:54272
	v_exp_f32_e32 v84, v84
	v_exp_f32_e32 v85, v85
	v_exp_f32_e32 v86, v86
	v_exp_f32_e32 v87, v87
	v_pk_add_f32 v[120:121], v[120:121], v[80:81]
	v_pk_add_f32 v[122:123], v[122:123], v[82:83]
	v_mfma_f32_32x32x64_f8f6f4 v[48:63], v[18:23], v[114:119], v[48:63] cbsz:2 blgp:2
	ds_read_b128 v[18:21], v124 offset:52224
	ds_read_b64 v[22:23], v125 offset:54784
	v_exp_f32_e32 v88, v88
	v_exp_f32_e32 v89, v89
	v_exp_f32_e32 v90, v90
	v_exp_f32_e32 v91, v91
	v_pk_add_f32 v[120:121], v[120:121], v[84:85]
	v_pk_add_f32 v[122:123], v[122:123], v[86:87]
	s_waitcnt lgkmcnt(8)
	s_nop 0
	v_mfma_f32_32x32x64_f8f6f4 v[64:79], v[24:29], v[96:101], 0 cbsz:2 blgp:2
	ds_read_b128 v[24:27], v124 offset:55296
	ds_read_b64 v[28:29], v125 offset:59392
	v_exp_f32_e32 v92, v92
	v_exp_f32_e32 v93, v93
	v_exp_f32_e32 v94, v94
	v_exp_f32_e32 v95, v95
	v_pk_add_f32 v[120:121], v[120:121], v[88:89]
	v_pk_add_f32 v[122:123], v[122:123], v[90:91]
	v_mfma_f32_32x32x64_f8f6f4 v[64:79], v[30:35], v[102:107], v[64:79] cbsz:2 blgp:2
	ds_read_b128 v[30:33], v124 offset:56320
	ds_read_b64 v[34:35], v125 offset:59904
	v_exp_f32_e32 v48, v48
	v_exp_f32_e32 v49, v49
	v_exp_f32_e32 v50, v50
	v_exp_f32_e32 v51, v51
	v_pk_add_f32 v[120:121], v[120:121], v[92:93]
	v_pk_add_f32 v[122:123], v[122:123], v[94:95]
	v_mfma_f32_32x32x64_f8f6f4 v[64:79], v[36:41], v[108:113], v[64:79] cbsz:2 blgp:2
	ds_read_b128 v[36:39], v124 offset:57344
	ds_read_b64 v[40:41], v125 offset:60416
	v_exp_f32_e32 v52, v52
	v_exp_f32_e32 v53, v53
	v_exp_f32_e32 v54, v54
	v_exp_f32_e32 v55, v55
	v_pk_add_f32 v[120:121], v[120:121], v[48:49]
	v_pk_add_f32 v[122:123], v[122:123], v[50:51]
	v_mfma_f32_32x32x64_f8f6f4 v[64:79], v[42:47], v[114:119], v[64:79] cbsz:2 blgp:2
	ds_read_b128 v[42:45], v124 offset:58368
	ds_read_b64 v[46:47], v125 offset:60928
	v_exp_f32_e32 v56, v56
	v_exp_f32_e32 v57, v57
	v_exp_f32_e32 v58, v58
	v_exp_f32_e32 v59, v59
	v_pk_add_f32 v[120:121], v[120:121], v[52:53]
	v_pk_add_f32 v[122:123], v[122:123], v[54:55]
	s_setprio 1
	s_waitcnt vmcnt(0) lgkmcnt(8)
	s_barrier
	s_nop 0
	v_mfma_f32_32x32x64_f8f6f4 v[80:95], v[0:5], v[96:101], 0 cbsz:2 blgp:2
	ds_read_b128 v[0:3], v124
	ds_read_b64 v[4:5], v125 offset:4096
	v_exp_f32_e32 v60, v60
	v_exp_f32_e32 v61, v61
	v_exp_f32_e32 v62, v62
	v_exp_f32_e32 v63, v63
	v_pk_add_f32 v[120:121], v[120:121], v[56:57]
	v_pk_add_f32 v[122:123], v[122:123], v[58:59]
	v_mfma_f32_32x32x64_f8f6f4 v[80:95], v[6:11], v[102:107], v[80:95] cbsz:2 blgp:2
	ds_read_b128 v[6:9], v124 offset:1024
	ds_read_b64 v[10:11], v125 offset:4608
	v_exp_f32_e32 v64, v64
	v_exp_f32_e32 v65, v65
	v_exp_f32_e32 v66, v66
	v_exp_f32_e32 v67, v67
	v_pk_add_f32 v[120:121], v[120:121], v[60:61]
	v_pk_add_f32 v[122:123], v[122:123], v[62:63]
	v_mfma_f32_32x32x64_f8f6f4 v[80:95], v[12:17], v[108:113], v[80:95] cbsz:2 blgp:2
	ds_read_b128 v[12:15], v124 offset:2048
	ds_read_b64 v[16:17], v125 offset:5120
	v_exp_f32_e32 v68, v68
	v_exp_f32_e32 v69, v69
	v_exp_f32_e32 v70, v70
	v_exp_f32_e32 v71, v71
	v_pk_add_f32 v[120:121], v[120:121], v[64:65]
	v_pk_add_f32 v[122:123], v[122:123], v[66:67]
	v_mfma_f32_32x32x64_f8f6f4 v[80:95], v[18:23], v[114:119], v[80:95] cbsz:2 blgp:2
	ds_read_b128 v[18:21], v124 offset:3072
	ds_read_b64 v[22:23], v125 offset:5632
	v_exp_f32_e32 v72, v72
	v_exp_f32_e32 v73, v73
	v_exp_f32_e32 v74, v74
	v_exp_f32_e32 v75, v75
	v_pk_add_f32 v[120:121], v[120:121], v[68:69]
	v_pk_add_f32 v[122:123], v[122:123], v[70:71]
	s_waitcnt lgkmcnt(8)
	s_nop 0
	v_mfma_f32_32x32x64_f8f6f4 v[48:63], v[24:29], v[96:101], 0 cbsz:2 blgp:2
	ds_read_b128 v[24:27], v124 offset:6144
	ds_read_b64 v[28:29], v125 offset:10240
	v_exp_f32_e32 v76, v76
	v_exp_f32_e32 v77, v77
	v_exp_f32_e32 v78, v78
	v_exp_f32_e32 v79, v79
	v_pk_add_f32 v[120:121], v[120:121], v[72:73]
	v_pk_add_f32 v[122:123], v[122:123], v[74:75]
	v_mfma_f32_32x32x64_f8f6f4 v[48:63], v[30:35], v[102:107], v[48:63] cbsz:2 blgp:2
	ds_read_b128 v[30:33], v124 offset:7168
	ds_read_b64 v[34:35], v125 offset:10752
	v_exp_f32_e32 v80, v80
	v_exp_f32_e32 v81, v81
	v_exp_f32_e32 v82, v82
	v_exp_f32_e32 v83, v83
	v_pk_add_f32 v[120:121], v[120:121], v[76:77]
	v_pk_add_f32 v[122:123], v[122:123], v[78:79]
	s_cmp_lg_u32 s8, 10
	s_cbranch_scc1 .Lmk_nosplit_a
	v_add_f32_e32 v127, v120, v121
	v_add_f32_e32 v126, v122, v123
	v_mov_b32_e32 v120, 0
	v_mov_b32_e32 v121, 0
	v_mov_b32_e32 v122, 0
	v_mov_b32_e32 v123, 0
	v_add_f32_e32 v127, v127, v126
.Lmk_nosplit_a:
	s_nop 0
	v_mfma_f32_32x32x64_f8f6f4 v[48:63], v[36:41], v[108:113], v[48:63] cbsz:2 blgp:2
	ds_read_b128 v[36:39], v124 offset:8192
	ds_read_b64 v[40:41], v125 offset:11264
	v_exp_f32_e32 v84, v84
	v_exp_f32_e32 v85, v85
	v_exp_f32_e32 v86, v86
	v_exp_f32_e32 v87, v87
	v_pk_add_f32 v[120:121], v[120:121], v[80:81]
	v_pk_add_f32 v[122:123], v[122:123], v[82:83]
	v_mfma_f32_32x32x64_f8f6f4 v[48:63], v[42:47], v[114:119], v[48:63] cbsz:2 blgp:2
	ds_read_b128 v[42:45], v124 offset:9216
	ds_read_b64 v[46:47], v125 offset:11776
	v_exp_f32_e32 v88, v88
	v_exp_f32_e32 v89, v89
	v_exp_f32_e32 v90, v90
	v_exp_f32_e32 v91, v91
	v_pk_add_f32 v[120:121], v[120:121], v[84:85]
	v_pk_add_f32 v[122:123], v[122:123], v[86:87]
	s_setprio 0
	s_waitcnt lgkmcnt(8)
	v_mfma_f32_32x32x64_f8f6f4 v[64:79], v[0:5], v[96:101], 0 cbsz:2 blgp:2
	v_exp_f32_e32 v92, v92
	v_exp_f32_e32 v93, v93
	v_exp_f32_e32 v94, v94
	v_exp_f32_e32 v95, v95
	v_pk_add_f32 v[120:121], v[120:121], v[88:89]
	v_pk_add_f32 v[122:123], v[122:123], v[90:91]
	v_mfma_f32_32x32x64_f8f6f4 v[64:79], v[6:11], v[102:107], v[64:79] cbsz:2 blgp:2
	v_exp_f32_e32 v48, v48
	v_exp_f32_e32 v49, v49
	v_exp_f32_e32 v50, v50
	v_exp_f32_e32 v51, v51
	v_pk_add_f32 v[120:121], v[120:121], v[92:93]
	v_pk_add_f32 v[122:123], v[122:123], v[94:95]
	v_mfma_f32_32x32x64_f8f6f4 v[64:79], v[12:17], v[108:113], v[64:79] cbsz:2 blgp:2
	v_exp_f32_e32 v52, v52
	v_exp_f32_e32 v53, v53
	v_exp_f32_e32 v54, v54
	v_exp_f32_e32 v55, v55
	v_pk_add_f32 v[120:121], v[120:121], v[48:49]
	v_pk_add_f32 v[122:123], v[122:123], v[50:51]
	v_mfma_f32_32x32x64_f8f6f4 v[64:79], v[18:23], v[114:119], v[64:79] cbsz:2 blgp:2
	v_exp_f32_e32 v56, v56
	v_exp_f32_e32 v57, v57
	v_exp_f32_e32 v58, v58
	v_exp_f32_e32 v59, v59
	v_pk_add_f32 v[120:121], v[120:121], v[52:53]
	v_pk_add_f32 v[122:123], v[122:123], v[54:55]
	s_waitcnt lgkmcnt(0)
	s_nop 0
	v_mfma_f32_32x32x64_f8f6f4 v[80:95], v[24:29], v[96:101], 0 cbsz:2 blgp:2
	v_exp_f32_e32 v60, v60
	v_exp_f32_e32 v61, v61
	v_exp_f32_e32 v62, v62
	v_exp_f32_e32 v63, v63
	v_pk_add_f32 v[120:121], v[120:121], v[56:57]
	v_pk_add_f32 v[122:123], v[122:123], v[58:59]
	v_mfma_f32_32x32x64_f8f6f4 v[80:95], v[30:35], v[102:107], v[80:95] cbsz:2 blgp:2
	v_exp_f32_e32 v64, v64
	v_exp_f32_e32 v65, v65
	v_exp_f32_e32 v66, v66
	v_exp_f32_e32 v67, v67
	v_pk_add_f32 v[120:121], v[120:121], v[60:61]
	v_pk_add_f32 v[122:123], v[122:123], v[62:63]
	v_mfma_f32_32x32x64_f8f6f4 v[80:95], v[36:41], v[108:113], v[80:95] cbsz:2 blgp:2
	v_exp_f32_e32 v68, v68
	v_exp_f32_e32 v69, v69
	v_exp_f32_e32 v70, v70
	v_exp_f32_e32 v71, v71
	v_pk_add_f32 v[120:121], v[120:121], v[64:65]
	v_pk_add_f32 v[122:123], v[122:123], v[66:67]
	v_mfma_f32_32x32x64_f8f6f4 v[80:95], v[42:47], v[114:119], v[80:95] cbsz:2 blgp:2
	v_exp_f32_e32 v72, v72
	v_exp_f32_e32 v73, v73
	v_exp_f32_e32 v74, v74
	v_exp_f32_e32 v75, v75
	v_pk_add_f32 v[120:121], v[120:121], v[68:69]
	v_pk_add_f32 v[122:123], v[122:123], v[70:71]
	v_exp_f32_e32 v76, v76
	v_exp_f32_e32 v77, v77
	v_exp_f32_e32 v78, v78
	v_exp_f32_e32 v79, v79
	v_pk_add_f32 v[120:121], v[120:121], v[72:73]
	v_pk_add_f32 v[122:123], v[122:123], v[74:75]
	s_nop 1
	v_exp_f32_e32 v80, v80
	v_exp_f32_e32 v81, v81
	v_exp_f32_e32 v82, v82
	v_exp_f32_e32 v83, v83
	v_pk_add_f32 v[120:121], v[120:121], v[76:77]
	v_pk_add_f32 v[122:123], v[122:123], v[78:79]
	v_exp_f32_e32 v84, v84
	v_exp_f32_e32 v85, v85
	v_exp_f32_e32 v86, v86
	v_exp_f32_e32 v87, v87
	v_pk_add_f32 v[120:121], v[120:121], v[80:81]
	v_pk_add_f32 v[122:123], v[122:123], v[82:83]
	v_exp_f32_e32 v88, v88
	v_exp_f32_e32 v89, v89
	v_exp_f32_e32 v90, v90
	v_exp_f32_e32 v91, v91
	v_pk_add_f32 v[120:121], v[120:121], v[84:85]
	v_pk_add_f32 v[122:123], v[122:123], v[86:87]
	v_exp_f32_e32 v92, v92
	v_exp_f32_e32 v93, v93
	v_exp_f32_e32 v94, v94
	v_exp_f32_e32 v95, v95
	v_pk_add_f32 v[120:121], v[120:121], v[88:89]
	v_pk_add_f32 v[122:123], v[122:123], v[90:91]
	v_pk_add_f32 v[120:121], v[120:121], v[92:93]
	v_pk_add_f32 v[122:123], v[122:123], v[94:95]
	v_add_f32_e32 v120, v120, v121
	v_add_f32_e32 v122, v122, v123
	v_lshrrev_b32_e32 v126, 2, v124
	v_add_f32_e32 v120, v120, v122
	v_xor_b32_e32 v125, 0x80, v126
	s_mov_b64 s[4:5], s[30:31]
	s_mov_b64 s[6:7], s[32:33]
	ds_bpermute_b32 v122, v125, v120
	ds_bpermute_b32 v123, v125, v127
	s_lshl_b32 s14, s14, 7
	v_add_u32_e32 v126, s14, v126
	v_cmp_gt_u32_e32 vcc, 0x200, v124
	s_and_saveexec_b64 s[16:17], vcc
	s_cbranch_execz .Lmk_end_a
	s_waitcnt lgkmcnt(0)
	v_add_f32_e32 v120, v120, v122
	v_add_f32_e32 v127, v127, v123
	s_cmp_lt_u32 s8, 10
	s_cbranch_scc1 .Lmk_pos_only_a
	s_cmp_eq_u32 s8, 10
	s_cbranch_scc0 .Lmk_neg_only_a
	global_atomic_add_f32 v126, v127, s[4:5]

.Lmk_vb:
	s_mov_b32 m0, s13
	s_nop 0
	global_load_lds_dwordx4 v124, s[10:11]
	global_load_dwordx4 v[96:99], v124, s[18:19]
	global_load_dwordx2 v[100:101], v125, s[22:23]
	global_load_dwordx4 v[102:105], v124, s[18:19] offset:1024
	global_load_dwordx2 v[106:107], v125, s[22:23] offset:512
	global_load_dwordx4 v[108:111], v124, s[18:19] offset:2048
	global_load_dwordx2 v[112:113], v125, s[22:23] offset:1024
	global_load_dwordx4 v[114:117], v124, s[18:19] offset:3072
	global_load_dwordx2 v[118:119], v125, s[22:23] offset:1536
	s_add_u32 s24, s10, 0x3000
	s_addc_u32 s25, s11, 0
	s_add_u32 s26, s13, 0x3000
	s_mov_b32 m0, s26
	s_nop 0
	global_load_lds_dwordx4 v124, s[24:25]
	s_add_u32 s24, s10, 0x6000
	s_addc_u32 s25, s11, 0
	s_add_u32 s26, s13, 0x6000
	s_mov_b32 m0, s26
	s_nop 0
	global_load_lds_dwordx4 v124, s[24:25]
	s_add_u32 s24, s10, 0x9000
	s_addc_u32 s25, s11, 0
	s_add_u32 s26, s13, 0x9000
	s_mov_b32 m0, s26
	s_nop 0
	global_load_lds_dwordx4 v124, s[24:25]
	s_add_u32 s24, s10, 0xc000
	s_addc_u32 s25, s11, 0
	s_add_u32 s26, s13, 0xc000
	s_mov_b32 m0, s26
	s_nop 0
	global_load_lds_dwordx4 v124, s[24:25]
	s_waitcnt vmcnt(4)
	s_barrier
	ds_read_b128 v[0:3], v124
	ds_read_b64 v[4:5], v125 offset:4096
	ds_read_b128 v[6:9], v124 offset:1024
	ds_read_b64 v[10:11], v125 offset:4608
	ds_read_b128 v[12:15], v124 offset:2048
	ds_read_b64 v[16:17], v125 offset:5120
	ds_read_b128 v[18:21], v124 offset:3072
	ds_read_b64 v[22:23], v125 offset:5632
	s_waitcnt lgkmcnt(0)
	s_setprio 3
	v_mfma_f32_32x32x64_f8f6f4 v[48:63], v[0:5], v[96:101], 0 cbsz:2 blgp:2
	ds_read_b128 v[24:27], v124 offset:6144
	ds_read_b64 v[28:29], v125 offset:10240
	v_mfma_f32_32x32x64_f8f6f4 v[48:63], v[6:11], v[102:107], v[48:63] cbsz:2 blgp:2
	ds_read_b128 v[30:33], v124 offset:7168
	ds_read_b64 v[34:35], v125 offset:10752
	v_mfma_f32_32x32x64_f8f6f4 v[48:63], v[12:17], v[108:113], v[48:63] cbsz:2 blgp:2
	ds_read_b128 v[36:39], v124 offset:8192
	ds_read_b64 v[40:41], v125 offset:11264
	v_mfma_f32_32x32x64_f8f6f4 v[48:63], v[18:23], v[114:119], v[48:63] cbsz:2 blgp:2
	ds_read_b128 v[42:45], v124 offset:9216
	ds_read_b64 v[46:47], v125 offset:11776
	s_waitcnt vmcnt(3) lgkmcnt(0)
	s_barrier
	s_add_u32 s24, s10, 0xf000
	s_addc_u32 s25, s11, 0
	s_mov_b32 m0, s13
	s_nop 0
	global_load_lds_dwordx4 v124, s[24:25]
	s_nop 0
	v_mfma_f32_32x32x64_f8f6f4 v[64:79], v[24:29], v[96:101], 0 cbsz:2 blgp:2
	ds_read_b128 v[0:3], v124 offset:12288
	ds_read_b64 v[4:5], v125 offset:16384
	ds_read_b128 v[6:9], v124 offset:13312
	ds_read_b64 v[10:11], v125 offset:16896
	ds_read_b128 v[24:27], v124 offset:18432
	ds_read_b64 v[28:29], v125 offset:22528
	v_mfma_f32_32x32x64_f8f6f4 v[64:79], v[30:35], v[102:107], v[64:79] cbsz:2 blgp:2
	ds_read_b128 v[12:15], v124 offset:14336
	ds_read_b64 v[16:17], v125 offset:17408
	ds_read_b128 v[18:21], v124 offset:15360
	ds_read_b64 v[22:23], v125 offset:17920
	ds_read_b128 v[30:33], v124 offset:19456
	ds_read_b64 v[34:35], v125 offset:23040
	v_exp_f32_e32 v48, v48
	v_exp_f32_e32 v49, v49
	v_exp_f32_e32 v50, v50
	v_exp_f32_e32 v51, v51
	v_mfma_f32_32x32x64_f8f6f4 v[64:79], v[36:41], v[108:113], v[64:79] cbsz:2 blgp:2
	ds_read_b128 v[36:39], v124 offset:20480
	ds_read_b64 v[40:41], v125 offset:23552
	v_exp_f32_e32 v52, v52
	v_exp_f32_e32 v53, v53
	v_exp_f32_e32 v54, v54
	v_exp_f32_e32 v55, v55
	v_pk_add_f32 v[120:121], v[120:121], v[48:49]
	v_pk_add_f32 v[122:123], v[122:123], v[50:51]
	v_mfma_f32_32x32x64_f8f6f4 v[64:79], v[42:47], v[114:119], v[64:79] cbsz:2 blgp:2
	ds_read_b128 v[42:45], v124 offset:21504
	ds_read_b64 v[46:47], v125 offset:24064
	v_exp_f32_e32 v56, v56
	v_exp_f32_e32 v57, v57
	v_exp_f32_e32 v58, v58
	v_exp_f32_e32 v59, v59
	v_pk_add_f32 v[120:121], v[120:121], v[52:53]
	v_pk_add_f32 v[122:123], v[122:123], v[54:55]
	s_waitcnt vmcnt(3) lgkmcnt(6)
	s_barrier
	v_mfma_f32_32x32x64_f8f6f4 v[80:95], v[0:5], v[96:101], 0 cbsz:2 blgp:2
	ds_read_b128 v[0:3], v124 offset:24576
	ds_read_b64 v[4:5], v125 offset:28672
	v_exp_f32_e32 v60, v60
	v_exp_f32_e32 v61, v61
	v_exp_f32_e32 v62, v62
	v_exp_f32_e32 v63, v63
	v_pk_add_f32 v[120:121], v[120:121], v[56:57]
	v_pk_add_f32 v[122:123], v[122:123], v[58:59]
	v_mfma_f32_32x32x64_f8f6f4 v[80:95], v[6:11], v[102:107], v[80:95] cbsz:2 blgp:2
	ds_read_b128 v[6:9], v124 offset:25600
	ds_read_b64 v[10:11], v125 offset:29184
	v_exp_f32_e32 v64, v64
	v_exp_f32_e32 v65, v65
	v_exp_f32_e32 v66, v66
	v_exp_f32_e32 v67, v67
	v_pk_add_f32 v[120:121], v[120:121], v[60:61]
	v_pk_add_f32 v[122:123], v[122:123], v[62:63]
	v_mfma_f32_32x32x64_f8f6f4 v[80:95], v[12:17], v[108:113], v[80:95] cbsz:2 blgp:2
	ds_read_b128 v[12:15], v124 offset:26624
	ds_read_b64 v[16:17], v125 offset:29696
	v_exp_f32_e32 v68, v68
	v_exp_f32_e32 v69, v69
	v_exp_f32_e32 v70, v70
	v_exp_f32_e32 v71, v71
	v_pk_add_f32 v[120:121], v[120:121], v[64:65]
	v_pk_add_f32 v[122:123], v[122:123], v[66:67]
	v_mfma_f32_32x32x64_f8f6f4 v[80:95], v[18:23], v[114:119], v[80:95] cbsz:2 blgp:2
	ds_read_b128 v[18:21], v124 offset:27648
	ds_read_b64 v[22:23], v125 offset:30208
	v_exp_f32_e32 v72, v72
	v_exp_f32_e32 v73, v73
	v_exp_f32_e32 v74, v74
	v_exp_f32_e32 v75, v75
	v_pk_add_f32 v[120:121], v[120:121], v[68:69]
	v_pk_add_f32 v[122:123], v[122:123], v[70:71]
	s_waitcnt lgkmcnt(8)
	s_nop 0
	v_mfma_f32_32x32x64_f8f6f4 v[48:63], v[24:29], v[96:101], 0 cbsz:2 blgp:2
	ds_read_b128 v[24:27], v124 offset:30720
	ds_read_b64 v[28:29], v125 offset:34816
	v_exp_f32_e32 v76, v76
	v_exp_f32_e32 v77, v77
	v_exp_f32_e32 v78, v78
	v_exp_f32_e32 v79, v79
	v_pk_add_f32 v[120:121], v[120:121], v[72:73]
	v_pk_add_f32 v[122:123], v[122:123], v[74:75]
	v_mfma_f32_32x32x64_f8f6f4 v[48:63], v[30:35], v[102:107], v[48:63] cbsz:2 blgp:2
	ds_read_b128 v[30:33], v124 offset:31744
	ds_read_b64 v[34:35], v125 offset:35328
	v_exp_f32_e32 v80, v80
	v_exp_f32_e32 v81, v81
	v_exp_f32_e32 v82, v82
	v_exp_f32_e32 v83, v83
	v_pk_add_f32 v[120:121], v[120:121], v[76:77]
	v_pk_add_f32 v[122:123], v[122:123], v[78:79]
	v_mfma_f32_32x32x64_f8f6f4 v[48:63], v[36:41], v[108:113], v[48:63] cbsz:2 blgp:2
	ds_read_b128 v[36:39], v124 offset:32768
	ds_read_b64 v[40:41], v125 offset:35840
	v_exp_f32_e32 v84, v84
	v_exp_f32_e32 v85, v85
	v_exp_f32_e32 v86, v86
	v_exp_f32_e32 v87, v87
	v_pk_add_f32 v[120:121], v[120:121], v[80:81]
	v_pk_add_f32 v[122:123], v[122:123], v[82:83]
	v_mfma_f32_32x32x64_f8f6f4 v[48:63], v[42:47], v[114:119], v[48:63] cbsz:2 blgp:2
	ds_read_b128 v[42:45], v124 offset:33792
	ds_read_b64 v[46:47], v125 offset:36352
	v_exp_f32_e32 v88, v88
	v_exp_f32_e32 v89, v89
	v_exp_f32_e32 v90, v90
	v_exp_f32_e32 v91, v91
	v_pk_add_f32 v[120:121], v[120:121], v[84:85]
	v_pk_add_f32 v[122:123], v[122:123], v[86:87]
	s_setprio 2
	s_waitcnt vmcnt(2) lgkmcnt(8)
	s_barrier
	s_nop 0
	v_mfma_f32_32x32x64_f8f6f4 v[64:79], v[0:5], v[96:101], 0 cbsz:2 blgp:2
	ds_read_b128 v[0:3], v124 offset:36864
	ds_read_b64 v[4:5], v125 offset:40960
	v_exp_f32_e32 v92, v92
	v_exp_f32_e32 v93, v93
	v_exp_f32_e32 v94, v94
	v_exp_f32_e32 v95, v95
	v_pk_add_f32 v[120:121], v[120:121], v[88:89]
	v_pk_add_f32 v[122:123], v[122:123], v[90:91]
	v_mfma_f32_32x32x64_f8f6f4 v[64:79], v[6:11], v[102:107], v[64:79] cbsz:2 blgp:2
	ds_read_b128 v[6:9], v124 offset:37888
	ds_read_b64 v[10:11], v125 offset:41472
	v_exp_f32_e32 v48, v48
	v_exp_f32_e32 v49, v49
	v_exp_f32_e32 v50, v50
	v_exp_f32_e32 v51, v51
	v_pk_add_f32 v[120:121], v[120:121], v[92:93]
	v_pk_add_f32 v[122:123], v[122:123], v[94:95]
	v_mfma_f32_32x32x64_f8f6f4 v[64:79], v[12:17], v[108:113], v[64:79] cbsz:2 blgp:2
	ds_read_b128 v[12:15], v124 offset:38912
	ds_read_b64 v[16:17], v125 offset:41984
	v_exp_f32_e32 v52, v52
	v_exp_f32_e32 v53, v53
	v_exp_f32_e32 v54, v54
	v_exp_f32_e32 v55, v55
	v_pk_add_f32 v[120:121], v[120:121], v[48:49]
	v_pk_add_f32 v[122:123], v[122:123], v[50:51]
	v_mfma_f32_32x32x64_f8f6f4 v[64:79], v[18:23], v[114:119], v[64:79] cbsz:2 blgp:2
	ds_read_b128 v[18:21], v124 offset:39936
	ds_read_b64 v[22:23], v125 offset:42496
	v_exp_f32_e32 v56, v56
	v_exp_f32_e32 v57, v57
	v_exp_f32_e32 v58, v58
	v_exp_f32_e32 v59, v59
	v_pk_add_f32 v[120:121], v[120:121], v[52:53]
	v_pk_add_f32 v[122:123], v[122:123], v[54:55]
	s_waitcnt lgkmcnt(8)
	s_nop 0
	v_mfma_f32_32x32x64_f8f6f4 v[80:95], v[24:29], v[96:101], 0 cbsz:2 blgp:2
	ds_read_b128 v[24:27], v124 offset:43008
	ds_read_b64 v[28:29], v125 offset:47104
	v_exp_f32_e32 v60, v60
	v_exp_f32_e32 v61, v61
	v_exp_f32_e32 v62, v62
	v_exp_f32_e32 v63, v63
	v_pk_add_f32 v[120:121], v[120:121], v[56:57]
	v_pk_add_f32 v[122:123], v[122:123], v[58:59]
	v_mfma_f32_32x32x64_f8f6f4 v[80:95], v[30:35], v[102:107], v[80:95] cbsz:2 blgp:2
	ds_read_b128 v[30:33], v124 offset:44032
	ds_read_b64 v[34:35], v125 offset:47616
	v_exp_f32_e32 v64, v64
	v_exp_f32_e32 v65, v65
	v_exp_f32_e32 v66, v66
	v_exp_f32_e32 v67, v67
	v_pk_add_f32 v[120:121], v[120:121], v[60:61]
	v_pk_add_f32 v[122:123], v[122:123], v[62:63]
	v_mfma_f32_32x32x64_f8f6f4 v[80:95], v[36:41], v[108:113], v[80:95] cbsz:2 blgp:2
	ds_read_b128 v[36:39], v124 offset:45056
	ds_read_b64 v[40:41], v125 offset:48128
	v_exp_f32_e32 v68, v68
	v_exp_f32_e32 v69, v69
	v_exp_f32_e32 v70, v70
	v_exp_f32_e32 v71, v71
	v_pk_add_f32 v[120:121], v[120:121], v[64:65]
	v_pk_add_f32 v[122:123], v[122:123], v[66:67]
	v_mfma_f32_32x32x64_f8f6f4 v[80:95], v[42:47], v[114:119], v[80:95] cbsz:2 blgp:2
	ds_read_b128 v[42:45], v124 offset:46080
	ds_read_b64 v[46:47], v125 offset:48640
	v_exp_f32_e32 v72, v72
	v_exp_f32_e32 v73, v73
	v_exp_f32_e32 v74, v74
	v_exp_f32_e32 v75, v75
	v_pk_add_f32 v[120:121], v[120:121], v[68:69]
	v_pk_add_f32 v[122:123], v[122:123], v[70:71]
	s_waitcnt vmcnt(1) lgkmcnt(8)
	s_barrier
	v_mfma_f32_32x32x64_f8f6f4 v[48:63], v[0:5], v[96:101], 0 cbsz:2 blgp:2
	ds_read_b128 v[0:3], v124 offset:49152
	ds_read_b64 v[4:5], v125 offset:53248
	v_exp_f32_e32 v76, v76
	v_exp_f32_e32 v77, v77
	v_exp_f32_e32 v78, v78
	v_exp_f32_e32 v79, v79
	v_pk_add_f32 v[120:121], v[120:121], v[72:73]
	v_pk_add_f32 v[122:123], v[122:123], v[74:75]
	v_mfma_f32_32x32x64_f8f6f4 v[48:63], v[6:11], v[102:107], v[48:63] cbsz:2 blgp:2
	ds_read_b128 v[6:9], v124 offset:50176
	ds_read_b64 v[10:11], v125 offset:53760
	v_exp_f32_e32 v80, v80
	v_exp_f32_e32 v81, v81
	v_exp_f32_e32 v82, v82
	v_exp_f32_e32 v83, v83
	v_pk_add_f32 v[120:121], v[120:121], v[76:77]
	v_pk_add_f32 v[122:123], v[122:123], v[78:79]
	v_mfma_f32_32x32x64_f8f6f4 v[48:63], v[12:17], v[108:113], v[48:63] cbsz:2 blgp:2
	ds_read_b128 v[12:15], v124 offset:51200
	ds_read_b64 v[16:17], v125 offset:54272
	v_exp_f32_e32 v84, v84
	v_exp_f32_e32 v85, v85
	v_exp_f32_e32 v86, v86
	v_exp_f32_e32 v87, v87
	v_pk_add_f32 v[120:121], v[120:121], v[80:81]
	v_pk_add_f32 v[122:123], v[122:123], v[82:83]
	v_mfma_f32_32x32x64_f8f6f4 v[48:63], v[18:23], v[114:119], v[48:63] cbsz:2 blgp:2
	ds_read_b128 v[18:21], v124 offset:52224
	ds_read_b64 v[22:23], v125 offset:54784
	v_exp_f32_e32 v88, v88
	v_exp_f32_e32 v89, v89
	v_exp_f32_e32 v90, v90
	v_exp_f32_e32 v91, v91
	v_pk_add_f32 v[120:121], v[120:121], v[84:85]
	v_pk_add_f32 v[122:123], v[122:123], v[86:87]
	s_waitcnt lgkmcnt(8)
	s_nop 0
	v_mfma_f32_32x32x64_f8f6f4 v[64:79], v[24:29], v[96:101], 0 cbsz:2 blgp:2
	ds_read_b128 v[24:27], v124 offset:55296
	ds_read_b64 v[28:29], v125 offset:59392
	v_exp_f32_e32 v92, v92
	v_exp_f32_e32 v93, v93
	v_exp_f32_e32 v94, v94
	v_exp_f32_e32 v95, v95
	v_pk_add_f32 v[120:121], v[120:121], v[88:89]
	v_pk_add_f32 v[122:123], v[122:123], v[90:91]
	v_mfma_f32_32x32x64_f8f6f4 v[64:79], v[30:35], v[102:107], v[64:79] cbsz:2 blgp:2
	ds_read_b128 v[30:33], v124 offset:56320
	ds_read_b64 v[34:35], v125 offset:59904
	v_exp_f32_e32 v48, v48
	v_exp_f32_e32 v49, v49
	v_exp_f32_e32 v50, v50
	v_exp_f32_e32 v51, v51
	v_pk_add_f32 v[120:121], v[120:121], v[92:93]
	v_pk_add_f32 v[122:123], v[122:123], v[94:95]
	v_mfma_f32_32x32x64_f8f6f4 v[64:79], v[36:41], v[108:113], v[64:79] cbsz:2 blgp:2
	ds_read_b128 v[36:39], v124 offset:57344
	ds_read_b64 v[40:41], v125 offset:60416
	v_exp_f32_e32 v52, v52
	v_exp_f32_e32 v53, v53
	v_exp_f32_e32 v54, v54
	v_exp_f32_e32 v55, v55
	v_pk_add_f32 v[120:121], v[120:121], v[48:49]
	v_pk_add_f32 v[122:123], v[122:123], v[50:51]
	v_mfma_f32_32x32x64_f8f6f4 v[64:79], v[42:47], v[114:119], v[64:79] cbsz:2 blgp:2
	ds_read_b128 v[42:45], v124 offset:58368
	ds_read_b64 v[46:47], v125 offset:60928
	v_exp_f32_e32 v56, v56
	v_exp_f32_e32 v57, v57
	v_exp_f32_e32 v58, v58
	v_exp_f32_e32 v59, v59
	v_pk_add_f32 v[120:121], v[120:121], v[52:53]
	v_pk_add_f32 v[122:123], v[122:123], v[54:55]
	s_setprio 1
	s_waitcnt vmcnt(0) lgkmcnt(8)
	s_barrier
	s_nop 0
	v_mfma_f32_32x32x64_f8f6f4 v[80:95], v[0:5], v[96:101], 0 cbsz:2 blgp:2
	ds_read_b128 v[0:3], v124
	ds_read_b64 v[4:5], v125 offset:4096
	v_exp_f32_e32 v60, v60
	v_exp_f32_e32 v61, v61
	v_exp_f32_e32 v62, v62
	v_exp_f32_e32 v63, v63
	v_pk_add_f32 v[120:121], v[120:121], v[56:57]
	v_pk_add_f32 v[122:123], v[122:123], v[58:59]
	v_mfma_f32_32x32x64_f8f6f4 v[80:95], v[6:11], v[102:107], v[80:95] cbsz:2 blgp:2
	ds_read_b128 v[6:9], v124 offset:1024
	ds_read_b64 v[10:11], v125 offset:4608
	v_exp_f32_e32 v64, v64
	v_exp_f32_e32 v65, v65
	v_exp_f32_e32 v66, v66
	v_exp_f32_e32 v67, v67
	v_pk_add_f32 v[120:121], v[120:121], v[60:61]
	v_pk_add_f32 v[122:123], v[122:123], v[62:63]
	v_mfma_f32_32x32x64_f8f6f4 v[80:95], v[12:17], v[108:113], v[80:95] cbsz:2 blgp:2
	ds_read_b128 v[12:15], v124 offset:2048
	ds_read_b64 v[16:17], v125 offset:5120
	v_exp_f32_e32 v68, v68
	v_exp_f32_e32 v69, v69
	v_exp_f32_e32 v70, v70
	v_exp_f32_e32 v71, v71
	v_pk_add_f32 v[120:121], v[120:121], v[64:65]
	v_pk_add_f32 v[122:123], v[122:123], v[66:67]
	v_mfma_f32_32x32x64_f8f6f4 v[80:95], v[18:23], v[114:119], v[80:95] cbsz:2 blgp:2
	ds_read_b128 v[18:21], v124 offset:3072
	ds_read_b64 v[22:23], v125 offset:5632
	v_exp_f32_e32 v72, v72
	v_exp_f32_e32 v73, v73
	v_exp_f32_e32 v74, v74
	v_exp_f32_e32 v75, v75
	v_pk_add_f32 v[120:121], v[120:121], v[68:69]
	v_pk_add_f32 v[122:123], v[122:123], v[70:71]
	s_waitcnt lgkmcnt(8)
	s_nop 0
	v_mfma_f32_32x32x64_f8f6f4 v[48:63], v[24:29], v[96:101], 0 cbsz:2 blgp:2
	ds_read_b128 v[24:27], v124 offset:6144
	ds_read_b64 v[28:29], v125 offset:10240
	v_exp_f32_e32 v76, v76
	v_exp_f32_e32 v77, v77
	v_exp_f32_e32 v78, v78
	v_exp_f32_e32 v79, v79
	v_pk_add_f32 v[120:121], v[120:121], v[72:73]
	v_pk_add_f32 v[122:123], v[122:123], v[74:75]
	v_mfma_f32_32x32x64_f8f6f4 v[48:63], v[30:35], v[102:107], v[48:63] cbsz:2 blgp:2
	ds_read_b128 v[30:33], v124 offset:7168
	ds_read_b64 v[34:35], v125 offset:10752
	v_exp_f32_e32 v80, v80
	v_exp_f32_e32 v81, v81
	v_exp_f32_e32 v82, v82
	v_exp_f32_e32 v83, v83
	v_pk_add_f32 v[120:121], v[120:121], v[76:77]
	v_pk_add_f32 v[122:123], v[122:123], v[78:79]
	s_cmp_lg_u32 s8, 10
	s_cbranch_scc1 .Lmk_nosplit_b
	v_add_f32_e32 v127, v120, v121
	v_add_f32_e32 v126, v122, v123
	v_mov_b32_e32 v120, 0
	v_mov_b32_e32 v121, 0
	v_mov_b32_e32 v122, 0
	v_mov_b32_e32 v123, 0
	v_add_f32_e32 v127, v127, v126
